# stack1
# baseline (speedup 1.0000x reference)
.LBB2_2:
	s_or_b64 exec, exec, s[12:13]
	v_lshrrev_b32_e32 v68, 7, v0
	s_lshl_b32 s0, s2, 4
	v_lshl_or_b32 v34, v68, 2, s0
	v_lshrrev_b32_e32 v2, 1, v0
	v_ashrrev_i32_e32 v35, 31, v34
	v_and_b32_e32 v69, 32, v2
	v_lshlrev_b64 v[2:3], 8, v[34:35]
	v_lshl_add_u64 v[2:3], s[4:5], 0, v[2:3]
	v_lshlrev_b32_e32 v66, 2, v69
	v_lshl_add_u64 v[2:3], v[2:3], 0, v[66:67]
	v_lshlrev_b32_e32 v36, 2, v1
	v_mov_b32_e32 v37, v67
	v_lshl_add_u64 v[2:3], v[2:3], 0, v[36:37]
	v_lshlrev_b32_e32 v38, 22, v72
	v_mov_b32_e32 v39, v67
	v_lshl_add_u64 v[4:5], v[2:3], 0, v[38:39]
	v_or_b32_e32 v40, 0x800000, v38
	v_mov_b32_e32 v41, v67
	global_load_dword v6, v[4:5], off
	v_lshl_add_u64 v[4:5], v[2:3], 0, v[40:41]
	v_or_b32_e32 v42, 0x1000000, v38
	v_mov_b32_e32 v43, v67
	global_load_dword v18, v[4:5], off
	v_lshl_add_u64 v[4:5], v[2:3], 0, v[42:43]
	v_or_b32_e32 v44, 0x1800000, v38
	v_mov_b32_e32 v45, v67
	global_load_dword v19, v[4:5], off
	v_lshl_add_u64 v[4:5], v[2:3], 0, v[44:45]
	v_or_b32_e32 v46, 0x2000000, v38
	v_mov_b32_e32 v47, v67
	global_load_dword v20, v[4:5], off
	v_lshl_add_u64 v[4:5], v[2:3], 0, v[46:47]
	v_or_b32_e32 v48, 0x2800000, v38
	v_mov_b32_e32 v49, v67
	global_load_dword v21, v[4:5], off
	v_lshl_add_u64 v[4:5], v[2:3], 0, v[48:49]
	v_or_b32_e32 v50, 0x3000000, v38
	v_mov_b32_e32 v51, v67
	global_load_dword v22, v[4:5], off
	v_lshl_add_u64 v[4:5], v[2:3], 0, v[50:51]
	v_or_b32_e32 v52, 0x3800000, v38
	v_mov_b32_e32 v53, v67
	global_load_dword v23, v[4:5], off
	v_lshl_add_u64 v[4:5], v[2:3], 0, v[52:53]
	v_or_b32_e32 v54, 0x4000000, v38
	v_mov_b32_e32 v55, v67
	global_load_dword v24, v[4:5], off
	v_lshl_add_u64 v[4:5], v[2:3], 0, v[54:55]
	v_or_b32_e32 v56, 0x4800000, v38
	v_mov_b32_e32 v57, v67
	global_load_dword v25, v[4:5], off
	v_lshl_add_u64 v[4:5], v[2:3], 0, v[56:57]
	v_or_b32_e32 v58, 0x5000000, v38
	v_mov_b32_e32 v59, v67
	global_load_dword v26, v[4:5], off
	v_lshl_add_u64 v[4:5], v[2:3], 0, v[58:59]
	v_or_b32_e32 v60, 0x5800000, v38
	v_mov_b32_e32 v61, v67
	s_mov_b64 s[6:7], 0x6000000
	global_load_dword v27, v[4:5], off
	v_lshl_add_u64 v[4:5], v[2:3], 0, v[60:61]
	v_lshl_add_u64 v[2:3], v[2:3], 0, s[6:7]
	global_load_dword v28, v[4:5], off
	global_load_dword v29, v[2:3], off
	v_or_b32_e32 v2, 1, v34
	v_ashrrev_i32_e32 v3, 31, v2
	v_lshlrev_b64 v[2:3], 8, v[2:3]
	v_lshl_add_u64 v[2:3], s[4:5], 0, v[2:3]
	v_lshl_add_u64 v[2:3], v[2:3], 0, v[66:67]
	v_lshl_add_u64 v[2:3], v[2:3], 0, v[36:37]
	v_lshl_add_u64 v[4:5], v[2:3], 0, v[38:39]
	global_load_dword v30, v[4:5], off
	v_lshl_add_u64 v[4:5], v[2:3], 0, v[40:41]
	global_load_dword v35, v[4:5], off
	v_lshl_add_u64 v[4:5], v[2:3], 0, v[42:43]
	global_load_dword v63, v[4:5], off
	v_lshl_add_u64 v[4:5], v[2:3], 0, v[44:45]
	global_load_dword v64, v[4:5], off
	v_lshl_add_u64 v[4:5], v[2:3], 0, v[46:47]
	global_load_dword v65, v[4:5], off
	v_lshl_add_u64 v[4:5], v[2:3], 0, v[48:49]
	global_load_dword v83, v[4:5], off
	v_lshl_add_u64 v[4:5], v[2:3], 0, v[50:51]
	global_load_dword v84, v[4:5], off
	v_lshl_add_u64 v[4:5], v[2:3], 0, v[52:53]
	global_load_dword v85, v[4:5], off
	v_lshl_add_u64 v[4:5], v[2:3], 0, v[54:55]
	global_load_dword v86, v[4:5], off
	v_lshl_add_u64 v[4:5], v[2:3], 0, v[56:57]
	global_load_dword v87, v[4:5], off
	v_lshl_add_u64 v[4:5], v[2:3], 0, v[58:59]
	global_load_dword v88, v[4:5], off
	v_lshl_add_u64 v[4:5], v[2:3], 0, v[60:61]
	global_load_dword v89, v[4:5], off
	v_lshl_add_u64 v[2:3], v[2:3], 0, s[6:7]
	global_load_dword v90, v[2:3], off
	s_waitcnt vmcnt(13)
	s_mov_b32 s0, 0xff61b1e6
	v_mfma_f32_32x32x2_f32 v[2:17], v62, v6, 0
	v_or_b32_e32 v1, v69, v1
	v_lshlrev_b32_e32 v1, 9, v1
	v_mfma_f32_32x32x2_f32 v[2:17], v82, v18, v[2:17]
	v_or_b32_e32 v18, 2, v34
	v_or_b32_e32 v34, 3, v34
	v_mfma_f32_32x32x2_f32 v[2:17], v81, v19, v[2:17]
	v_ashrrev_i32_e32 v19, 31, v18
	v_lshlrev_b64 v[18:19], 8, v[18:19]
	v_lshl_add_u64 v[18:19], s[4:5], 0, v[18:19]
	v_lshl_add_u64 v[18:19], v[18:19], 0, v[66:67]
	v_lshl_add_u64 v[18:19], v[18:19], 0, v[36:37]
	v_mfma_f32_32x32x2_f32 v[2:17], v80, v20, v[2:17]
	v_mfma_f32_32x32x2_f32 v[2:17], v79, v21, v[2:17]
	v_lshl_add_u64 v[20:21], v[18:19], 0, v[38:39]
	global_load_dword v91, v[20:21], off
	v_lshl_add_u64 v[20:21], v[18:19], 0, v[40:41]
	global_load_dword v92, v[20:21], off
	v_lshl_add_u64 v[20:21], v[18:19], 0, v[42:43]
	global_load_dword v93, v[20:21], off
	v_lshl_add_u64 v[20:21], v[18:19], 0, v[44:45]
	global_load_dword v94, v[20:21], off
	v_lshl_add_u64 v[20:21], v[18:19], 0, v[46:47]
	global_load_dword v95, v[20:21], off
	v_lshl_add_u64 v[20:21], v[18:19], 0, v[48:49]
	global_load_dword v96, v[20:21], off
	v_lshl_add_u64 v[20:21], v[18:19], 0, v[50:51]
	global_load_dword v97, v[20:21], off
	v_lshl_add_u64 v[20:21], v[18:19], 0, v[52:53]
	v_mfma_f32_32x32x2_f32 v[2:17], v78, v22, v[2:17]
	global_load_dword v98, v[20:21], off
	v_lshl_add_u64 v[20:21], v[18:19], 0, v[54:55]
	global_load_dword v99, v[20:21], off
	v_lshl_add_u64 v[20:21], v[18:19], 0, v[56:57]
	global_load_dword v100, v[20:21], off
	v_lshl_add_u64 v[20:21], v[18:19], 0, v[58:59]
	global_load_dword v101, v[20:21], off
	v_lshl_add_u64 v[20:21], v[18:19], 0, v[60:61]
	global_load_dword v102, v[20:21], off
	v_lshl_add_u64 v[18:19], v[18:19], 0, s[6:7]
	global_load_dword v103, v[18:19], off
	s_waitcnt vmcnt(13)
	v_mfma_f32_32x32x2_f32 v[2:17], v77, v23, v[2:17]
	v_mfma_f32_32x32x2_f32 v[2:17], v76, v24, v[2:17]
	v_mfma_f32_32x32x2_f32 v[2:17], v75, v25, v[2:17]
	v_mfma_f32_32x32x2_f32 v[2:17], v74, v26, v[2:17]
	v_mfma_f32_32x32x2_f32 v[2:17], v73, v27, v[2:17]
	v_mfma_f32_32x32x2_f32 v[2:17], v71, v28, v[2:17]
	v_mfma_f32_32x32x2_f32 v[2:17], v70, v29, v[2:17]
	v_mfma_f32_32x32x2_f32 v[18:33], v62, v30, 0
	v_mfma_f32_32x32x2_f32 v[18:33], v82, v35, v[18:33]
	v_ashrrev_i32_e32 v35, 31, v34
	v_lshlrev_b64 v[34:35], 8, v[34:35]
	v_lshl_add_u64 v[34:35], s[4:5], 0, v[34:35]
	v_lshl_add_u64 v[34:35], v[34:35], 0, v[66:67]
	v_lshl_add_u64 v[34:35], v[34:35], 0, v[36:37]
	v_lshl_add_u64 v[36:37], v[34:35], 0, v[38:39]
	v_mfma_f32_32x32x2_f32 v[18:33], v81, v63, v[18:33]
	global_load_dword v63, v[36:37], off
	v_lshl_add_u64 v[36:37], v[34:35], 0, v[40:41]
	global_load_dword v66, v[36:37], off
	v_lshl_add_u64 v[36:37], v[34:35], 0, v[42:43]
	v_mfma_f32_32x32x2_f32 v[18:33], v80, v64, v[18:33]
	v_mfma_f32_32x32x2_f32 v[18:33], v79, v65, v[18:33]
	v_mfma_f32_32x32x2_f32 v[18:33], v78, v83, v[18:33]
	global_load_dword v83, v[36:37], off
	v_lshl_add_u64 v[36:37], v[34:35], 0, v[44:45]
	v_mfma_f32_32x32x2_f32 v[18:33], v77, v84, v[18:33]
	global_load_dword v84, v[36:37], off
	v_lshl_add_u64 v[36:37], v[34:35], 0, v[46:47]
	v_mfma_f32_32x32x2_f32 v[18:33], v76, v85, v[18:33]
	global_load_dword v85, v[36:37], off
	v_lshl_add_u64 v[36:37], v[34:35], 0, v[48:49]
	v_mfma_f32_32x32x2_f32 v[18:33], v75, v86, v[18:33]
	global_load_dword v86, v[36:37], off
	v_lshl_add_u64 v[36:37], v[34:35], 0, v[50:51]
	v_mfma_f32_32x32x2_f32 v[18:33], v74, v87, v[18:33]
	global_load_dword v87, v[36:37], off
	v_lshl_add_u64 v[36:37], v[34:35], 0, v[52:53]
	v_mfma_f32_32x32x2_f32 v[18:33], v73, v88, v[18:33]
	global_load_dword v88, v[36:37], off
	v_lshl_add_u64 v[36:37], v[34:35], 0, v[54:55]
	v_mfma_f32_32x32x2_f32 v[18:33], v71, v89, v[18:33]
	global_load_dword v89, v[36:37], off
	v_lshl_add_u64 v[36:37], v[34:35], 0, v[56:57]
	v_mfma_f32_32x32x2_f32 v[18:33], v70, v90, v[18:33]
	global_load_dword v90, v[36:37], off
	v_lshl_add_u64 v[36:37], v[34:35], 0, v[58:59]
	global_load_dword v104, v[36:37], off
	v_lshl_add_u64 v[36:37], v[34:35], 0, v[60:61]
	global_load_dword v105, v[36:37], off
	v_lshl_add_u64 v[34:35], v[34:35], 0, s[6:7]
	global_load_dword v106, v[34:35], off
	s_waitcnt vmcnt(13)
	s_nop 14
	v_max3_f32 v2, v2, s0, v18
	s_waitcnt vmcnt(0)
	v_mfma_f32_32x32x2_f32 v[34:49], v62, v91, 0
	v_max3_f32 v3, v3, s0, v19
	v_max3_f32 v4, v4, s0, v20
	v_max3_f32 v5, v5, s0, v21
	v_max3_f32 v6, v6, s0, v22
	v_max3_f32 v7, v7, s0, v23
	v_max3_f32 v8, v8, s0, v24
	v_max3_f32 v9, v9, s0, v25
	v_lshlrev_b32_e32 v18, 5, v68
	v_max3_f32 v10, v10, s0, v26
	v_max3_f32 v11, v11, s0, v27
	v_max3_f32 v12, v12, s0, v28
	v_max3_f32 v13, v13, s0, v29
	v_max3_f32 v14, v14, s0, v30
	v_max3_f32 v15, v15, s0, v31
	v_max3_f32 v16, v16, s0, v32
	v_mfma_f32_32x32x2_f32 v[50:65], v62, v63, 0
	v_max3_f32 v17, v17, s0, v33
	s_lshl_b32 s0, s2, 2
	s_mov_b32 s2, 0x7f000
	v_mfma_f32_32x32x2_f32 v[34:49], v82, v92, v[34:49]
	v_mfma_f32_32x32x2_f32 v[50:65], v82, v66, v[50:65]
	v_lshlrev_b32_e32 v66, 4, v72
	v_or3_b32 v1, v1, v18, v66
	v_mfma_f32_32x32x2_f32 v[34:49], v81, v93, v[34:49]
	v_mfma_f32_32x32x2_f32 v[50:65], v81, v83, v[50:65]
	v_mfma_f32_32x32x2_f32 v[34:49], v80, v94, v[34:49]
	v_mfma_f32_32x32x2_f32 v[50:65], v80, v84, v[50:65]
	v_mfma_f32_32x32x2_f32 v[34:49], v79, v95, v[34:49]
	v_mfma_f32_32x32x2_f32 v[50:65], v79, v85, v[50:65]
	v_mfma_f32_32x32x2_f32 v[34:49], v78, v96, v[34:49]
	v_mfma_f32_32x32x2_f32 v[50:65], v78, v86, v[50:65]
	v_mfma_f32_32x32x2_f32 v[34:49], v77, v97, v[34:49]
	v_mfma_f32_32x32x2_f32 v[50:65], v77, v87, v[50:65]
	v_mfma_f32_32x32x2_f32 v[34:49], v76, v98, v[34:49]
	v_mfma_f32_32x32x2_f32 v[50:65], v76, v88, v[50:65]
	v_mfma_f32_32x32x2_f32 v[34:49], v75, v99, v[34:49]
	v_mfma_f32_32x32x2_f32 v[50:65], v75, v89, v[50:65]
	v_mfma_f32_32x32x2_f32 v[34:49], v74, v100, v[34:49]
	v_mfma_f32_32x32x2_f32 v[50:65], v74, v90, v[50:65]
	global_load_dwordx4 v[74:77], v66, s[8:9]
	global_load_dwordx4 v[78:81], v66, s[8:9] offset:32
	global_load_dwordx4 v[82:85], v66, s[8:9] offset:64
	global_load_dwordx4 v[86:89], v66, s[8:9] offset:96
	v_mfma_f32_32x32x2_f32 v[34:49], v73, v101, v[34:49]
	v_mfma_f32_32x32x2_f32 v[50:65], v73, v104, v[50:65]
	v_mfma_f32_32x32x2_f32 v[34:49], v71, v102, v[34:49]
	v_mfma_f32_32x32x2_f32 v[50:65], v71, v105, v[50:65]
	v_mfma_f32_32x32x2_f32 v[34:49], v70, v103, v[34:49]
	v_mfma_f32_32x32x2_f32 v[50:65], v70, v106, v[50:65]
	s_nop 15
	s_nop 1
	v_max3_f32 v2, v2, v34, v50
	v_max3_f32 v3, v3, v35, v51
	v_max3_f32 v4, v4, v36, v52
	v_max3_f32 v5, v5, v37, v53
	s_waitcnt vmcnt(3)
	v_add_f32_e32 v2, v2, v74
	v_add_f32_e32 v3, v3, v75
	v_add_f32_e32 v4, v4, v76
	v_add_f32_e32 v5, v5, v77
	v_max3_f32 v6, v6, v38, v54
	v_max3_f32 v7, v7, v39, v55
	v_max3_f32 v8, v8, v40, v56
	v_max3_f32 v9, v9, v41, v57
	v_max_f32_e32 v2, 0, v2
	v_max_f32_e32 v3, 0, v3
	v_max_f32_e32 v4, 0, v4
	v_max_f32_e32 v5, 0, v5
	ds_write_b128 v1, v[2:5]
	s_waitcnt vmcnt(2)
	v_add_f32_e32 v2, v6, v78
	v_add_f32_e32 v3, v7, v79
	v_add_f32_e32 v4, v8, v80
	v_add_f32_e32 v5, v9, v81
	v_max3_f32 v10, v10, v42, v58
	v_max3_f32 v11, v11, v43, v59
	v_max3_f32 v12, v12, v44, v60
	v_max3_f32 v13, v13, v45, v61
	v_max_f32_e32 v2, 0, v2
	v_max_f32_e32 v3, 0, v3
	v_max_f32_e32 v4, 0, v4
	v_max_f32_e32 v5, 0, v5
	ds_write_b128 v1, v[2:5] offset:128
	s_waitcnt vmcnt(1)
	v_add_f32_e32 v2, v10, v82
	v_add_f32_e32 v3, v11, v83
	v_add_f32_e32 v4, v12, v84
	v_add_f32_e32 v5, v13, v85
	v_max3_f32 v14, v14, v46, v62
	v_max3_f32 v15, v15, v47, v63
	v_max3_f32 v16, v16, v48, v64
	v_max3_f32 v17, v17, v49, v65
	v_max_f32_e32 v2, 0, v2
	v_max_f32_e32 v3, 0, v3
	v_max_f32_e32 v4, 0, v4
	v_max_f32_e32 v5, 0, v5
	ds_write_b128 v1, v[2:5] offset:256
	s_waitcnt vmcnt(0)
	v_add_f32_e32 v2, v14, v86
	v_add_f32_e32 v3, v15, v87
	v_add_f32_e32 v4, v16, v88
	v_add_f32_e32 v5, v17, v89
	v_max_f32_e32 v2, 0, v2
	v_max_f32_e32 v3, 0, v3
	v_max_f32_e32 v4, 0, v4
	v_max_f32_e32 v5, 0, v5
	v_lshlrev_b32_e32 v12, 4, v0
	ds_write_b128 v1, v[2:5] offset:384
	s_waitcnt lgkmcnt(0)
	s_barrier
	v_and_b32_e32 v66, 0x70, v12
	v_lshlrev_b32_e32 v13, 9, v0
	ds_read_b128 v[0:3], v12
	v_lshl_add_u64 v[8:9], s[10:11], 0, v[66:67]
	v_and_b32_e32 v66, 0x3f000, v13
	v_lshl_add_u64 v[4:5], v[66:67], 0, s[0:1]
	v_lshlrev_b64 v[4:5], 5, v[4:5]
	v_lshl_add_u64 v[10:11], v[8:9], 0, v[4:5]
	ds_read_b128 v[4:7], v12 offset:8192
	s_waitcnt lgkmcnt(1)
	global_store_dwordx4 v[10:11], v[0:3], off
	s_nop 1
	v_mov_b32_e32 v0, 0x40000
	v_bitop3_b32 v66, v13, s2, v0 bitop3:0xc8
	v_lshl_add_u64 v[0:1], v[66:67], 0, s[0:1]
	v_lshlrev_b64 v[0:1], 5, v[0:1]
	v_lshl_add_u64 v[0:1], v[8:9], 0, v[0:1]
	s_waitcnt lgkmcnt(0)
	global_store_dwordx4 v[0:1], v[4:7], off
	s_mov_b32 s2, 0xbf000
	v_mov_b32_e32 v0, 0x80000
	v_bitop3_b32 v66, v13, s2, v0 bitop3:0xc8
	ds_read_b128 v[0:3], v12 offset:16384
	v_lshl_add_u64 v[4:5], v[66:67], 0, s[0:1]
	v_lshlrev_b64 v[4:5], 5, v[4:5]
	v_lshl_add_u64 v[10:11], v[8:9], 0, v[4:5]
	ds_read_b128 v[4:7], v12 offset:24576
	s_waitcnt lgkmcnt(1)
	global_store_dwordx4 v[10:11], v[0:3], off
	s_mov_b32 s2, 0xff000
	s_nop 0
	v_mov_b32_e32 v0, 0xc0000
	v_bitop3_b32 v66, v13, s2, v0 bitop3:0xc8
	v_lshl_add_u64 v[0:1], v[66:67], 0, s[0:1]
	v_lshlrev_b64 v[0:1], 5, v[0:1]
	v_lshl_add_u64 v[0:1], v[8:9], 0, v[0:1]
	s_waitcnt lgkmcnt(0)
	global_store_dwordx4 v[0:1], v[4:7], off
	s_endpgm
